# overlap across the barrier: the 16 closing v_exp of a tile body run behind the barrier and the next body's first four K-fragment reads (5 of 6 body boundaries; exit body keeps a copy at the drain head
# baseline (speedup 1.0000x reference)
.LBB0_792:
	s_waitcnt vmcnt(4) lgkmcnt(0)
	s_barrier
	ds_read_b128 v[64:67], v134 offset:50176
	ds_read_b128 v[68:71], v134 offset:58368
	ds_read_b128 v[200:203], v135 offset:50176
	ds_read_b128 v[204:207], v135 offset:58368
	v_exp_f32_e32 v197, v96
	v_exp_f32_e32 v208, v97
	v_exp_f32_e32 v209, v98
	v_exp_f32_e32 v210, v99
	v_exp_f32_e32 v211, v100
	v_exp_f32_e32 v220, v101
	v_exp_f32_e32 v221, v102
	v_exp_f32_e32 v222, v103
	v_exp_f32_e32 v223, v104
	v_exp_f32_e32 v224, v105
	v_exp_f32_e32 v225, v106
	v_exp_f32_e32 v226, v107
	v_exp_f32_e32 v227, v108
	v_exp_f32_e32 v228, v109
	v_exp_f32_e32 v229, v110
	v_exp_f32_e32 v230, v111
	v_exp_f32_e32 v231, v87
	s_waitcnt lgkmcnt(2)
	v_mfma_f32_32x32x16_bf16 v[96:111], v[64:67], v[122:125], 0
	v_exp_f32_e32 v232, v88
	v_exp_f32_e32 v233, v89
	v_exp_f32_e32 v234, v90
	v_exp_f32_e32 v235, v91
	v_exp_f32_e32 v236, v92
	v_exp_f32_e32 v237, v93
	v_exp_f32_e32 v238, v94
	v_mfma_f32_32x32x16_bf16 v[64:79], v[68:71], v[122:125], 0
	v_exp_f32_e32 v95, v95
	s_waitcnt lgkmcnt(0)
	v_mfma_f32_32x32x16_bf16 v[96:111], v[200:203], v[126:129], v[96:111]
	v_mfma_f32_32x32x16_bf16 v[64:79], v[204:207], v[126:129], v[64:79]
	ds_read_b128 v[200:203], v136 offset:50176
	ds_read_b128 v[204:207], v136 offset:58368
	s_waitcnt lgkmcnt(0)
	v_mfma_f32_32x32x16_bf16 v[96:111], v[200:203], v[118:121], v[96:111]
	v_mfma_f32_32x32x16_bf16 v[64:79], v[204:207], v[118:121], v[64:79]
	ds_read_b128 v[200:203], v137 offset:50176
	ds_read_b128 v[204:207], v137 offset:58368
	s_waitcnt lgkmcnt(0)
	v_mfma_f32_32x32x16_bf16 v[96:111], v[200:203], v[114:117], v[96:111]
	v_exp_f32_e32 v201, v80
	v_add_f32_e32 v80, v208, v197
	v_add_f32_e32 v199, v209, v210
	v_add_f32_e32 v80, v211, v80
	v_add_f32_e32 v199, v220, v199
	v_add_f32_e32 v80, v221, v80
	v_add_f32_e32 v199, v222, v199
	v_add_f32_e32 v80, v223, v80
	v_add_f32_e32 v199, v224, v199
	v_add_f32_e32 v80, v225, v80
	v_add_f32_e32 v199, v226, v199
	v_add_f32_e32 v80, v227, v80
	v_exp_f32_e32 v202, v81
	v_add_f32_e32 v199, v228, v199
	v_exp_f32_e32 v203, v82
	v_add_f32_e32 v80, v229, v80
	v_mfma_f32_32x32x16_bf16 v[64:79], v[204:207], v[114:117], v[64:79]
	v_exp_f32_e32 v204, v83
	v_add_f32_e32 v199, v230, v199
	v_exp_f32_e32 v205, v84
	v_add_f32_e32 v80, v201, v80
	v_exp_f32_e32 v206, v85
	v_add_f32_e32 v199, v202, v199
	v_exp_f32_e32 v207, v86
	v_add_f32_e32 v80, v203, v80
	v_add_f32_e32 v199, v204, v199
	v_add_f32_e32 v80, v205, v80
	v_add_f32_e32 v199, v206, v199
	v_add_f32_e32 v80, v207, v80
	v_add_f32_e32 v199, v231, v199
	v_add_f32_e32 v80, v232, v80
	v_add_f32_e32 v199, v233, v199
	v_add_f32_e32 v80, v234, v80
	v_add_f32_e32 v199, v235, v199
	v_add_f32_e32 v80, v236, v80
	v_add_f32_e32 v199, v237, v199
	v_add_f32_e32 v80, v238, v80
	v_add_f32_e32 v199, v95, v199
	v_add_f32_e32 v199, v199, v80
	v_cvt_pk_bf16_f32 v80, v197, v208
	v_cvt_pk_bf16_f32 v81, v209, v210
	v_cvt_pk_bf16_f32 v82, v211, v220
	v_cvt_pk_bf16_f32 v83, v221, v222
	v_cvt_pk_bf16_f32 v84, v223, v224
	v_cvt_pk_bf16_f32 v85, v225, v226
	v_cvt_pk_bf16_f32 v86, v227, v228
	v_cvt_pk_bf16_f32 v87, v229, v230
	v_cvt_pk_bf16_f32 v88, v201, v202
	v_cvt_pk_bf16_f32 v89, v203, v204
	v_cvt_pk_bf16_f32 v90, v205, v206
	v_cvt_pk_bf16_f32 v91, v207, v231
	v_cvt_pk_bf16_f32 v92, v232, v233
	v_cvt_pk_bf16_f32 v93, v234, v235
	v_cvt_pk_bf16_f32 v94, v236, v237
	v_cvt_pk_bf16_f32 v95, v238, v95
	s_add_i32 m0, s84, 0x400
	s_add_u32 s66, s78, s65
	s_addc_u32 s67, s79, 0
	global_load_lds_dwordx4 v185, s[66:67]
	s_add_i32 m0, s84, 0x2400
	s_add_i32 s64, s65, 0x60000
	global_load_lds_dwordx4 v184, s[66:67]
	s_cmp_eq_u32 s55, 29
	s_cselect_b32 s64, s89, s64
	s_add_i32 m0, s84, 0x10400
	s_add_u32 s70, s80, s64
	s_addc_u32 s71, s81, 0
	global_load_lds_dwordx4 v183, s[70:71]
	s_add_i32 m0, s84, 0x12400
	s_mov_b32 s65, s64
	global_load_lds_dwordx4 v182, s[70:71]

.LBB0_799:
	v_fma_f32 v80, v193, v179, v195
	v_fma_f32 v179, v80, v198, v199
	s_cmp_gt_u32 s55, 32
	s_waitcnt vmcnt(4) lgkmcnt(0)
	s_barrier
	s_cbranch_scc1 .LBB0_803
	s_add_i32 s55, s55, 2
	v_mov_b32_e32 v193, v197
	ds_read_b128 v[80:83], v130 offset:50176
	ds_read_b128 v[84:87], v130 offset:58368
	ds_read_b128 v[196:199], v131 offset:50176
	ds_read_b128 v[200:203], v131 offset:58368
	v_exp_f32_e32 v159, v96
	v_exp_f32_e32 v161, v97
	v_exp_f32_e32 v157, v98
	v_exp_f32_e32 v160, v99
	v_exp_f32_e32 v155, v100
	v_exp_f32_e32 v158, v101
	v_exp_f32_e32 v154, v102
	v_exp_f32_e32 v156, v103
	v_exp_f32_e32 v151, v104
	v_exp_f32_e32 v153, v105
	v_exp_f32_e32 v149, v106
	v_exp_f32_e32 v152, v107
	v_exp_f32_e32 v147, v108
	v_exp_f32_e32 v150, v109
	v_exp_f32_e32 v146, v110
	v_exp_f32_e32 v148, v111
	s_waitcnt lgkmcnt(2)
	v_mfma_f32_32x32x16_bf16 v[96:111], v[80:83], v[122:125], 0
	v_exp_f32_e32 v204, v72
	v_exp_f32_e32 v205, v73
	v_exp_f32_e32 v206, v74
	v_exp_f32_e32 v207, v75
	v_exp_f32_e32 v208, v76
	v_exp_f32_e32 v209, v77
	v_mfma_f32_32x32x16_bf16 v[80:95], v[84:87], v[122:125], 0
	v_exp_f32_e32 v210, v78
	v_exp_f32_e32 v79, v79
	s_waitcnt lgkmcnt(0)
	v_mfma_f32_32x32x16_bf16 v[96:111], v[196:199], v[126:129], v[96:111]
	v_mfma_f32_32x32x16_bf16 v[80:95], v[200:203], v[126:129], v[80:95]
	ds_read_b128 v[196:199], v132 offset:50176
	ds_read_b128 v[200:203], v132 offset:58368
	s_waitcnt lgkmcnt(0)
	v_mfma_f32_32x32x16_bf16 v[96:111], v[196:199], v[118:121], v[96:111]
	v_mfma_f32_32x32x16_bf16 v[80:95], v[200:203], v[118:121], v[80:95]
	ds_read_b128 v[196:199], v133 offset:50176
	ds_read_b128 v[200:203], v133 offset:58368
	v_exp_f32_e32 v180, v64
	v_add_f32_e32 v64, v161, v159
	v_add_f32_e32 v195, v157, v160
	v_add_f32_e32 v64, v155, v64
	v_add_f32_e32 v195, v158, v195
	v_add_f32_e32 v64, v154, v64
	v_add_f32_e32 v195, v156, v195
	v_add_f32_e32 v64, v151, v64
	v_add_f32_e32 v195, v153, v195
	v_add_f32_e32 v64, v149, v64
	v_add_f32_e32 v195, v152, v195
	v_add_f32_e32 v64, v147, v64
	s_waitcnt lgkmcnt(0)
	v_mfma_f32_32x32x16_bf16 v[96:111], v[196:199], v[114:117], v[96:111]
	v_exp_f32_e32 v197, v65
	v_add_f32_e32 v195, v150, v195
	v_exp_f32_e32 v198, v66
	v_add_f32_e32 v64, v146, v64
	v_exp_f32_e32 v199, v67
	v_add_f32_e32 v195, v148, v195
	v_add_f32_e32 v64, v180, v64
	v_mfma_f32_32x32x16_bf16 v[80:95], v[200:203], v[114:117], v[80:95]
	v_exp_f32_e32 v200, v68
	v_exp_f32_e32 v201, v69
	v_add_f32_e32 v195, v197, v195
	v_exp_f32_e32 v202, v70
	v_add_f32_e32 v64, v198, v64
	v_exp_f32_e32 v203, v71
	v_add_f32_e32 v195, v199, v195
	v_add_f32_e32 v64, v200, v64
	v_add_f32_e32 v195, v201, v195
	v_add_f32_e32 v64, v202, v64
	v_add_f32_e32 v195, v203, v195
	v_add_f32_e32 v64, v204, v64
	v_add_f32_e32 v195, v205, v195
	v_add_f32_e32 v64, v206, v64
	v_add_f32_e32 v195, v207, v195
	v_add_f32_e32 v64, v208, v64
	v_add_f32_e32 v195, v209, v195
	v_add_f32_e32 v64, v210, v64
	v_add_f32_e32 v195, v79, v195
	v_add_f32_e32 v195, v195, v64
	v_cvt_pk_bf16_f32 v64, v159, v161
	v_cvt_pk_bf16_f32 v65, v157, v160
	v_cvt_pk_bf16_f32 v66, v155, v158
	v_cvt_pk_bf16_f32 v67, v154, v156
	v_cvt_pk_bf16_f32 v68, v151, v153
	v_cvt_pk_bf16_f32 v69, v149, v152
	v_cvt_pk_bf16_f32 v70, v147, v150
	v_cvt_pk_bf16_f32 v71, v146, v148
	v_cvt_pk_bf16_f32 v72, v180, v197
	v_cvt_pk_bf16_f32 v73, v198, v199
	v_cvt_pk_bf16_f32 v74, v200, v201
	v_cvt_pk_bf16_f32 v75, v202, v203
	v_cvt_pk_bf16_f32 v76, v204, v205
	v_cvt_pk_bf16_f32 v77, v206, v207
	v_cvt_pk_bf16_f32 v78, v208, v209
	v_cvt_pk_bf16_f32 v79, v210, v79
	s_add_i32 m0, s84, 0x4400
	s_add_u32 s66, s78, s65
	s_addc_u32 s67, s79, 0
	global_load_lds_dwordx4 v185, s[66:67]
	s_add_i32 m0, s84, 0x6400
	s_add_i32 s64, s65, 0x60000
	global_load_lds_dwordx4 v184, s[66:67]
	s_add_i32 m0, s84, 0x14400
	s_add_u32 s70, s80, s64
	s_addc_u32 s71, s81, 0
	global_load_lds_dwordx4 v183, s[70:71]
	s_add_i32 m0, s84, 0x16400
	s_mov_b32 s65, s64
	global_load_lds_dwordx4 v182, s[70:71]
	ds_read_b64_tr_b16 v[198:199], v192 offset:33792
	ds_read_b64_tr_b16 v[200:201], v192 offset:35840
	ds_read_b64_tr_b16 v[202:203], v192 offset:37888
	ds_read_b64_tr_b16 v[204:205], v192 offset:39936
	ds_read_b64_tr_b16 v[206:207], v192 offset:41984
	ds_read_b64_tr_b16 v[208:209], v192 offset:44032
	ds_read_b64_tr_b16 v[222:223], v192 offset:46080
	ds_read_b64_tr_b16 v[224:225], v192 offset:48128
	s_waitcnt lgkmcnt(0)
	v_mfma_f32_32x32x16_bf16 v[0:15], v[64:67], v[198:201], v[0:15]
	ds_read_b64_tr_b16 v[198:199], v192 offset:34304
	ds_read_b64_tr_b16 v[200:201], v192 offset:36352
	ds_read_b64_tr_b16 v[138:139], v192 offset:42496
	ds_read_b64_tr_b16 v[140:141], v192 offset:44544
	v_mfma_f32_32x32x16_bf16 v[0:15], v[68:71], v[202:205], v[0:15]
	ds_read_b64_tr_b16 v[202:203], v192 offset:38400
	ds_read_b64_tr_b16 v[204:205], v192 offset:40448
	ds_read_b64_tr_b16 v[142:143], v192 offset:46592
	ds_read_b64_tr_b16 v[144:145], v192 offset:48640
	v_mfma_f32_32x32x16_bf16 v[0:15], v[72:75], v[206:209], v[0:15]
	v_mfma_f32_32x32x16_bf16 v[0:15], v[76:79], v[222:225], v[0:15]
	s_waitcnt lgkmcnt(0)
	v_mfma_f32_32x32x16_bf16 v[48:63], v[64:67], v[198:201], v[48:63]
	ds_read_b64_tr_b16 v[198:199], v192 offset:34816
	ds_read_b64_tr_b16 v[200:201], v192 offset:36864
	ds_read_b64_tr_b16 v[206:207], v192 offset:43008
	ds_read_b64_tr_b16 v[208:209], v192 offset:45056
	v_mfma_f32_32x32x16_bf16 v[48:63], v[68:71], v[202:205], v[48:63]
	ds_read_b64_tr_b16 v[202:203], v192 offset:38912
	ds_read_b64_tr_b16 v[204:205], v192 offset:40960
	ds_read_b64_tr_b16 v[222:223], v192 offset:47104
	ds_read_b64_tr_b16 v[224:225], v192 offset:49152
	v_mfma_f32_32x32x16_bf16 v[48:63], v[72:75], v[138:141], v[48:63]
	v_mfma_f32_32x32x16_bf16 v[48:63], v[76:79], v[142:145], v[48:63]
	s_waitcnt lgkmcnt(0)
	v_mfma_f32_32x32x16_bf16 v[32:47], v[64:67], v[198:201], v[32:47]
	ds_read_b64_tr_b16 v[198:199], v192 offset:35328
	ds_read_b64_tr_b16 v[200:201], v192 offset:37376
	ds_read_b64_tr_b16 v[138:139], v192 offset:43520
	ds_read_b64_tr_b16 v[140:141], v192 offset:45568
	v_mfma_f32_32x32x16_bf16 v[32:47], v[68:71], v[202:205], v[32:47]
	ds_read_b64_tr_b16 v[202:203], v192 offset:39424
	ds_read_b64_tr_b16 v[204:205], v192 offset:41472
	ds_read_b64_tr_b16 v[142:143], v192 offset:47616
	ds_read_b64_tr_b16 v[144:145], v192 offset:49664
	v_mfma_f32_32x32x16_bf16 v[32:47], v[72:75], v[206:209], v[32:47]
	v_mfma_f32_32x32x16_bf16 v[32:47], v[76:79], v[222:225], v[32:47]
	s_waitcnt lgkmcnt(0)
	v_mfma_f32_32x32x16_bf16 v[16:31], v[64:67], v[198:201], v[16:31]
	v_max_f32_e32 v64, v96, v97
	v_max3_f32 v65, v80, v81, v82
	v_max3_f32 v64, v64, v98, v99
	v_max3_f32 v65, v65, v83, v84
	v_max3_f32 v64, v64, v100, v101
	v_mfma_f32_32x32x16_bf16 v[16:31], v[68:71], v[202:205], v[16:31]
	v_max3_f32 v65, v65, v85, v86
	v_max3_f32 v64, v64, v102, v103
	v_max3_f32 v65, v65, v87, v88
	v_max3_f32 v64, v64, v104, v105
	v_max3_f32 v65, v65, v89, v90
	v_max3_f32 v64, v64, v106, v107
	v_max3_f32 v65, v65, v91, v92
	v_mfma_f32_32x32x16_bf16 v[16:31], v[72:75], v[138:141], v[16:31]
	v_max3_f32 v64, v64, v108, v109
	v_max3_f32 v65, v65, v93, v94
	v_max3_f32 v64, v64, v110, v111
	v_max3_f32 v64, v64, v65, v95
	v_mov_b32_e32 v198, 1.0
	v_mfma_f32_32x32x16_bf16 v[16:31], v[76:79], v[142:145], v[16:31]
	v_cmp_ge_f32_e64 s[0:1], s56, v64
	s_cmp_eq_u64 s[0:1], exec
	s_cbranch_scc1 .Lc1_792
	s_branch .Lc1_801

.Lc1_792:
	s_waitcnt vmcnt(4) lgkmcnt(0)
	s_barrier
	ds_read_b128 v[64:67], v134 offset:33792
	ds_read_b128 v[68:71], v134 offset:41984
	ds_read_b128 v[200:203], v135 offset:33792
	ds_read_b128 v[204:207], v135 offset:41984
	v_exp_f32_e32 v197, v96
	v_exp_f32_e32 v208, v97
	v_exp_f32_e32 v209, v98
	v_exp_f32_e32 v210, v99
	v_exp_f32_e32 v211, v100
	v_exp_f32_e32 v220, v101
	v_exp_f32_e32 v221, v102
	v_exp_f32_e32 v222, v103
	v_exp_f32_e32 v223, v104
	v_exp_f32_e32 v224, v105
	v_exp_f32_e32 v225, v106
	v_exp_f32_e32 v226, v107
	v_exp_f32_e32 v227, v108
	v_exp_f32_e32 v228, v109
	v_exp_f32_e32 v229, v110
	v_exp_f32_e32 v230, v111
	v_exp_f32_e32 v231, v87
	s_waitcnt lgkmcnt(2)
	v_mfma_f32_32x32x16_bf16 v[96:111], v[64:67], v[122:125], 0
	v_exp_f32_e32 v232, v88
	v_exp_f32_e32 v233, v89
	v_exp_f32_e32 v234, v90
	v_exp_f32_e32 v235, v91
	v_exp_f32_e32 v236, v92
	v_exp_f32_e32 v237, v93
	v_exp_f32_e32 v238, v94
	v_mfma_f32_32x32x16_bf16 v[64:79], v[68:71], v[122:125], 0
	v_exp_f32_e32 v95, v95
	s_waitcnt lgkmcnt(0)
	v_mfma_f32_32x32x16_bf16 v[96:111], v[200:203], v[126:129], v[96:111]
	v_mfma_f32_32x32x16_bf16 v[64:79], v[204:207], v[126:129], v[64:79]
	ds_read_b128 v[200:203], v136 offset:33792
	ds_read_b128 v[204:207], v136 offset:41984
	s_waitcnt lgkmcnt(0)
	v_mfma_f32_32x32x16_bf16 v[96:111], v[200:203], v[118:121], v[96:111]
	v_mfma_f32_32x32x16_bf16 v[64:79], v[204:207], v[118:121], v[64:79]
	ds_read_b128 v[200:203], v137 offset:33792
	ds_read_b128 v[204:207], v137 offset:41984
	s_waitcnt lgkmcnt(0)
	v_mfma_f32_32x32x16_bf16 v[96:111], v[200:203], v[114:117], v[96:111]
	v_exp_f32_e32 v201, v80
	v_add_f32_e32 v80, v208, v197
	v_add_f32_e32 v199, v209, v210
	v_add_f32_e32 v80, v211, v80
	v_add_f32_e32 v199, v220, v199
	v_add_f32_e32 v80, v221, v80
	v_add_f32_e32 v199, v222, v199
	v_add_f32_e32 v80, v223, v80
	v_add_f32_e32 v199, v224, v199
	v_add_f32_e32 v80, v225, v80
	v_add_f32_e32 v199, v226, v199
	v_add_f32_e32 v80, v227, v80
	v_exp_f32_e32 v202, v81
	v_add_f32_e32 v199, v228, v199
	v_exp_f32_e32 v203, v82
	v_add_f32_e32 v80, v229, v80
	v_mfma_f32_32x32x16_bf16 v[64:79], v[204:207], v[114:117], v[64:79]
	v_exp_f32_e32 v204, v83
	v_add_f32_e32 v199, v230, v199
	v_exp_f32_e32 v205, v84
	v_add_f32_e32 v80, v201, v80
	v_exp_f32_e32 v206, v85
	v_add_f32_e32 v199, v202, v199
	v_exp_f32_e32 v207, v86
	v_add_f32_e32 v80, v203, v80
	v_add_f32_e32 v199, v204, v199
	v_add_f32_e32 v80, v205, v80
	v_add_f32_e32 v199, v206, v199
	v_add_f32_e32 v80, v207, v80
	v_add_f32_e32 v199, v231, v199
	v_add_f32_e32 v80, v232, v80
	v_add_f32_e32 v199, v233, v199
	v_add_f32_e32 v80, v234, v80
	v_add_f32_e32 v199, v235, v199
	v_add_f32_e32 v80, v236, v80
	v_add_f32_e32 v199, v237, v199
	v_add_f32_e32 v80, v238, v80
	v_add_f32_e32 v199, v95, v199
	v_add_f32_e32 v199, v199, v80
	v_cvt_pk_bf16_f32 v80, v197, v208
	v_cvt_pk_bf16_f32 v81, v209, v210
	v_cvt_pk_bf16_f32 v82, v211, v220
	v_cvt_pk_bf16_f32 v83, v221, v222
	v_cvt_pk_bf16_f32 v84, v223, v224
	v_cvt_pk_bf16_f32 v85, v225, v226
	v_cvt_pk_bf16_f32 v86, v227, v228
	v_cvt_pk_bf16_f32 v87, v229, v230
	v_cvt_pk_bf16_f32 v88, v201, v202
	v_cvt_pk_bf16_f32 v89, v203, v204
	v_cvt_pk_bf16_f32 v90, v205, v206
	v_cvt_pk_bf16_f32 v91, v207, v231
	v_cvt_pk_bf16_f32 v92, v232, v233
	v_cvt_pk_bf16_f32 v93, v234, v235
	v_cvt_pk_bf16_f32 v94, v236, v237
	v_cvt_pk_bf16_f32 v95, v238, v95
	s_add_i32 m0, s84, 0x8400
	s_add_u32 s66, s78, s65
	s_addc_u32 s67, s79, 0
	global_load_lds_dwordx4 v185, s[66:67]
	s_add_i32 m0, s84, 0xa400
	s_add_i32 s64, s65, 0x60000
	global_load_lds_dwordx4 v184, s[66:67]
	s_cmp_eq_u32 s55, 29
	s_cselect_b32 s64, s89, s64
	s_add_i32 m0, s84, 0xc400
	s_add_u32 s70, s80, s64
	s_addc_u32 s71, s81, 0
	global_load_lds_dwordx4 v183, s[70:71]
	s_add_i32 m0, s84, 0xe400
	s_mov_b32 s65, s64
	global_load_lds_dwordx4 v182, s[70:71]

.Lc1_799:
	v_fma_f32 v80, v193, v179, v195
	v_fma_f32 v179, v80, v198, v199
	s_cmp_gt_u32 s55, 32
	s_waitcnt vmcnt(4) lgkmcnt(0)
	s_barrier
	s_cbranch_scc1 .LBB0_803
	s_add_i32 s55, s55, 2
	v_mov_b32_e32 v193, v197
	ds_read_b128 v[80:83], v134 offset:50176
	ds_read_b128 v[84:87], v134 offset:58368
	ds_read_b128 v[196:199], v135 offset:50176
	ds_read_b128 v[200:203], v135 offset:58368
	v_exp_f32_e32 v159, v96
	v_exp_f32_e32 v161, v97
	v_exp_f32_e32 v157, v98
	v_exp_f32_e32 v160, v99
	v_exp_f32_e32 v155, v100
	v_exp_f32_e32 v158, v101
	v_exp_f32_e32 v154, v102
	v_exp_f32_e32 v156, v103
	v_exp_f32_e32 v151, v104
	v_exp_f32_e32 v153, v105
	v_exp_f32_e32 v149, v106
	v_exp_f32_e32 v152, v107
	v_exp_f32_e32 v147, v108
	v_exp_f32_e32 v150, v109
	v_exp_f32_e32 v146, v110
	v_exp_f32_e32 v148, v111
	s_waitcnt lgkmcnt(2)
	v_mfma_f32_32x32x16_bf16 v[96:111], v[80:83], v[122:125], 0
	v_exp_f32_e32 v204, v72
	v_exp_f32_e32 v205, v73
	v_exp_f32_e32 v206, v74
	v_exp_f32_e32 v207, v75
	v_exp_f32_e32 v208, v76
	v_exp_f32_e32 v209, v77
	v_mfma_f32_32x32x16_bf16 v[80:95], v[84:87], v[122:125], 0
	v_exp_f32_e32 v210, v78
	v_exp_f32_e32 v79, v79
	s_waitcnt lgkmcnt(0)
	v_mfma_f32_32x32x16_bf16 v[96:111], v[196:199], v[126:129], v[96:111]
	v_mfma_f32_32x32x16_bf16 v[80:95], v[200:203], v[126:129], v[80:95]
	ds_read_b128 v[196:199], v136 offset:50176
	ds_read_b128 v[200:203], v136 offset:58368
	s_waitcnt lgkmcnt(0)
	v_mfma_f32_32x32x16_bf16 v[96:111], v[196:199], v[118:121], v[96:111]
	v_mfma_f32_32x32x16_bf16 v[80:95], v[200:203], v[118:121], v[80:95]
	ds_read_b128 v[196:199], v137 offset:50176
	ds_read_b128 v[200:203], v137 offset:58368
	v_exp_f32_e32 v180, v64
	v_add_f32_e32 v64, v161, v159
	v_add_f32_e32 v195, v157, v160
	v_add_f32_e32 v64, v155, v64
	v_add_f32_e32 v195, v158, v195
	v_add_f32_e32 v64, v154, v64
	v_add_f32_e32 v195, v156, v195
	v_add_f32_e32 v64, v151, v64
	v_add_f32_e32 v195, v153, v195
	v_add_f32_e32 v64, v149, v64
	v_add_f32_e32 v195, v152, v195
	v_add_f32_e32 v64, v147, v64
	s_waitcnt lgkmcnt(0)
	v_mfma_f32_32x32x16_bf16 v[96:111], v[196:199], v[114:117], v[96:111]
	v_exp_f32_e32 v197, v65
	v_add_f32_e32 v195, v150, v195
	v_exp_f32_e32 v198, v66
	v_add_f32_e32 v64, v146, v64
	v_exp_f32_e32 v199, v67
	v_add_f32_e32 v195, v148, v195
	v_add_f32_e32 v64, v180, v64
	v_mfma_f32_32x32x16_bf16 v[80:95], v[200:203], v[114:117], v[80:95]
	v_exp_f32_e32 v200, v68
	v_exp_f32_e32 v201, v69
	v_add_f32_e32 v195, v197, v195
	v_exp_f32_e32 v202, v70
	v_add_f32_e32 v64, v198, v64
	v_exp_f32_e32 v203, v71
	v_add_f32_e32 v195, v199, v195
	v_add_f32_e32 v64, v200, v64
	v_add_f32_e32 v195, v201, v195
	v_add_f32_e32 v64, v202, v64
	v_add_f32_e32 v195, v203, v195
	v_add_f32_e32 v64, v204, v64
	v_add_f32_e32 v195, v205, v195
	v_add_f32_e32 v64, v206, v64
	v_add_f32_e32 v195, v207, v195
	v_add_f32_e32 v64, v208, v64
	v_add_f32_e32 v195, v209, v195
	v_add_f32_e32 v64, v210, v64
	v_add_f32_e32 v195, v79, v195
	v_add_f32_e32 v195, v195, v64
	v_cvt_pk_bf16_f32 v64, v159, v161
	v_cvt_pk_bf16_f32 v65, v157, v160
	v_cvt_pk_bf16_f32 v66, v155, v158
	v_cvt_pk_bf16_f32 v67, v154, v156
	v_cvt_pk_bf16_f32 v68, v151, v153
	v_cvt_pk_bf16_f32 v69, v149, v152
	v_cvt_pk_bf16_f32 v70, v147, v150
	v_cvt_pk_bf16_f32 v71, v146, v148
	v_cvt_pk_bf16_f32 v72, v180, v197
	v_cvt_pk_bf16_f32 v73, v198, v199
	v_cvt_pk_bf16_f32 v74, v200, v201
	v_cvt_pk_bf16_f32 v75, v202, v203
	v_cvt_pk_bf16_f32 v76, v204, v205
	v_cvt_pk_bf16_f32 v77, v206, v207
	v_cvt_pk_bf16_f32 v78, v208, v209
	v_cvt_pk_bf16_f32 v79, v210, v79
	s_add_i32 m0, s84, 0x400
	s_add_u32 s66, s78, s65
	s_addc_u32 s67, s79, 0
	global_load_lds_dwordx4 v185, s[66:67]
	s_add_i32 m0, s84, 0x2400
	s_add_i32 s64, s65, 0x60000
	global_load_lds_dwordx4 v184, s[66:67]
	s_add_i32 m0, s84, 0x10400
	s_add_u32 s70, s80, s64
	s_addc_u32 s71, s81, 0
	global_load_lds_dwordx4 v183, s[70:71]
	s_add_i32 m0, s84, 0x12400
	s_mov_b32 s65, s64
	global_load_lds_dwordx4 v182, s[70:71]
	ds_read_b64_tr_b16 v[198:199], v192 offset:17408
	ds_read_b64_tr_b16 v[200:201], v192 offset:19456
	ds_read_b64_tr_b16 v[202:203], v192 offset:21504
	ds_read_b64_tr_b16 v[204:205], v192 offset:23552
	ds_read_b64_tr_b16 v[206:207], v192 offset:25600
	ds_read_b64_tr_b16 v[208:209], v192 offset:27648
	ds_read_b64_tr_b16 v[222:223], v192 offset:29696
	ds_read_b64_tr_b16 v[224:225], v192 offset:31744
	s_waitcnt lgkmcnt(0)
	v_mfma_f32_32x32x16_bf16 v[0:15], v[64:67], v[198:201], v[0:15]
	ds_read_b64_tr_b16 v[198:199], v192 offset:17920
	ds_read_b64_tr_b16 v[200:201], v192 offset:19968
	ds_read_b64_tr_b16 v[138:139], v192 offset:26112
	ds_read_b64_tr_b16 v[140:141], v192 offset:28160
	v_mfma_f32_32x32x16_bf16 v[0:15], v[68:71], v[202:205], v[0:15]
	ds_read_b64_tr_b16 v[202:203], v192 offset:22016
	ds_read_b64_tr_b16 v[204:205], v192 offset:24064
	ds_read_b64_tr_b16 v[142:143], v192 offset:30208
	ds_read_b64_tr_b16 v[144:145], v192 offset:32256
	v_mfma_f32_32x32x16_bf16 v[0:15], v[72:75], v[206:209], v[0:15]
	v_mfma_f32_32x32x16_bf16 v[0:15], v[76:79], v[222:225], v[0:15]
	s_waitcnt lgkmcnt(0)
	v_mfma_f32_32x32x16_bf16 v[48:63], v[64:67], v[198:201], v[48:63]
	ds_read_b64_tr_b16 v[198:199], v192 offset:18432
	ds_read_b64_tr_b16 v[200:201], v192 offset:20480
	ds_read_b64_tr_b16 v[206:207], v192 offset:26624
	ds_read_b64_tr_b16 v[208:209], v192 offset:28672
	v_mfma_f32_32x32x16_bf16 v[48:63], v[68:71], v[202:205], v[48:63]
	ds_read_b64_tr_b16 v[202:203], v192 offset:22528
	ds_read_b64_tr_b16 v[204:205], v192 offset:24576
	ds_read_b64_tr_b16 v[222:223], v192 offset:30720
	ds_read_b64_tr_b16 v[224:225], v192 offset:32768
	v_mfma_f32_32x32x16_bf16 v[48:63], v[72:75], v[138:141], v[48:63]
	v_mfma_f32_32x32x16_bf16 v[48:63], v[76:79], v[142:145], v[48:63]
	s_waitcnt lgkmcnt(0)
	v_mfma_f32_32x32x16_bf16 v[32:47], v[64:67], v[198:201], v[32:47]
	ds_read_b64_tr_b16 v[198:199], v192 offset:18944
	ds_read_b64_tr_b16 v[200:201], v192 offset:20992
	ds_read_b64_tr_b16 v[138:139], v192 offset:27136
	ds_read_b64_tr_b16 v[140:141], v192 offset:29184
	v_mfma_f32_32x32x16_bf16 v[32:47], v[68:71], v[202:205], v[32:47]
	ds_read_b64_tr_b16 v[202:203], v192 offset:23040
	ds_read_b64_tr_b16 v[204:205], v192 offset:25088
	ds_read_b64_tr_b16 v[142:143], v192 offset:31232
	ds_read_b64_tr_b16 v[144:145], v192 offset:33280
	v_mfma_f32_32x32x16_bf16 v[32:47], v[72:75], v[206:209], v[32:47]
	v_mfma_f32_32x32x16_bf16 v[32:47], v[76:79], v[222:225], v[32:47]
	s_waitcnt lgkmcnt(0)
	v_mfma_f32_32x32x16_bf16 v[16:31], v[64:67], v[198:201], v[16:31]
	v_max_f32_e32 v64, v96, v97
	v_max3_f32 v65, v80, v81, v82
	v_max3_f32 v64, v64, v98, v99
	v_max3_f32 v65, v65, v83, v84
	v_max3_f32 v64, v64, v100, v101
	v_mfma_f32_32x32x16_bf16 v[16:31], v[68:71], v[202:205], v[16:31]
	v_max3_f32 v65, v65, v85, v86
	v_max3_f32 v64, v64, v102, v103
	v_max3_f32 v65, v65, v87, v88
	v_max3_f32 v64, v64, v104, v105
	v_max3_f32 v65, v65, v89, v90
	v_max3_f32 v64, v64, v106, v107
	v_max3_f32 v65, v65, v91, v92
	v_mfma_f32_32x32x16_bf16 v[16:31], v[72:75], v[138:141], v[16:31]
	v_max3_f32 v64, v64, v108, v109
	v_max3_f32 v65, v65, v93, v94
	v_max3_f32 v64, v64, v110, v111
	v_max3_f32 v64, v64, v65, v95
	v_mov_b32_e32 v198, 1.0
	v_mfma_f32_32x32x16_bf16 v[16:31], v[76:79], v[142:145], v[16:31]
	v_cmp_ge_f32_e64 s[0:1], s56, v64
	s_cmp_eq_u64 s[0:1], exec
	s_cbranch_scc1 .Lc2_792
	s_branch .Lc2_801

.Lc2_792:
	s_waitcnt vmcnt(4) lgkmcnt(0)
	s_barrier
	ds_read_b128 v[64:67], v130 offset:50176
	ds_read_b128 v[68:71], v130 offset:58368
	ds_read_b128 v[200:203], v131 offset:50176
	ds_read_b128 v[204:207], v131 offset:58368
	v_exp_f32_e32 v197, v96
	v_exp_f32_e32 v208, v97
	v_exp_f32_e32 v209, v98
	v_exp_f32_e32 v210, v99
	v_exp_f32_e32 v211, v100
	v_exp_f32_e32 v220, v101
	v_exp_f32_e32 v221, v102
	v_exp_f32_e32 v222, v103
	v_exp_f32_e32 v223, v104
	v_exp_f32_e32 v224, v105
	v_exp_f32_e32 v225, v106
	v_exp_f32_e32 v226, v107
	v_exp_f32_e32 v227, v108
	v_exp_f32_e32 v228, v109
	v_exp_f32_e32 v229, v110
	v_exp_f32_e32 v230, v111
	v_exp_f32_e32 v231, v87
	s_waitcnt lgkmcnt(2)
	v_mfma_f32_32x32x16_bf16 v[96:111], v[64:67], v[122:125], 0
	v_exp_f32_e32 v232, v88
	v_exp_f32_e32 v233, v89
	v_exp_f32_e32 v234, v90
	v_exp_f32_e32 v235, v91
	v_exp_f32_e32 v236, v92
	v_exp_f32_e32 v237, v93
	v_exp_f32_e32 v238, v94
	v_mfma_f32_32x32x16_bf16 v[64:79], v[68:71], v[122:125], 0
	v_exp_f32_e32 v95, v95
	s_waitcnt lgkmcnt(0)
	v_mfma_f32_32x32x16_bf16 v[96:111], v[200:203], v[126:129], v[96:111]
	v_mfma_f32_32x32x16_bf16 v[64:79], v[204:207], v[126:129], v[64:79]
	ds_read_b128 v[200:203], v132 offset:50176
	ds_read_b128 v[204:207], v132 offset:58368
	s_waitcnt lgkmcnt(0)
	v_mfma_f32_32x32x16_bf16 v[96:111], v[200:203], v[118:121], v[96:111]
	v_mfma_f32_32x32x16_bf16 v[64:79], v[204:207], v[118:121], v[64:79]
	ds_read_b128 v[200:203], v133 offset:50176
	ds_read_b128 v[204:207], v133 offset:58368
	s_waitcnt lgkmcnt(0)
	v_mfma_f32_32x32x16_bf16 v[96:111], v[200:203], v[114:117], v[96:111]
	v_exp_f32_e32 v201, v80
	v_add_f32_e32 v80, v208, v197
	v_add_f32_e32 v199, v209, v210
	v_add_f32_e32 v80, v211, v80
	v_add_f32_e32 v199, v220, v199
	v_add_f32_e32 v80, v221, v80
	v_add_f32_e32 v199, v222, v199
	v_add_f32_e32 v80, v223, v80
	v_add_f32_e32 v199, v224, v199
	v_add_f32_e32 v80, v225, v80
	v_add_f32_e32 v199, v226, v199
	v_add_f32_e32 v80, v227, v80
	v_exp_f32_e32 v202, v81
	v_add_f32_e32 v199, v228, v199
	v_exp_f32_e32 v203, v82
	v_add_f32_e32 v80, v229, v80
	v_mfma_f32_32x32x16_bf16 v[64:79], v[204:207], v[114:117], v[64:79]
	v_exp_f32_e32 v204, v83
	v_add_f32_e32 v199, v230, v199
	v_exp_f32_e32 v205, v84
	v_add_f32_e32 v80, v201, v80
	v_exp_f32_e32 v206, v85
	v_add_f32_e32 v199, v202, v199
	v_exp_f32_e32 v207, v86
	v_add_f32_e32 v80, v203, v80
	v_add_f32_e32 v199, v204, v199
	v_add_f32_e32 v80, v205, v80
	v_add_f32_e32 v199, v206, v199
	v_add_f32_e32 v80, v207, v80
	v_add_f32_e32 v199, v231, v199
	v_add_f32_e32 v80, v232, v80
	v_add_f32_e32 v199, v233, v199
	v_add_f32_e32 v80, v234, v80
	v_add_f32_e32 v199, v235, v199
	v_add_f32_e32 v80, v236, v80
	v_add_f32_e32 v199, v237, v199
	v_add_f32_e32 v80, v238, v80
	v_add_f32_e32 v199, v95, v199
	v_add_f32_e32 v199, v199, v80
	v_cvt_pk_bf16_f32 v80, v197, v208
	v_cvt_pk_bf16_f32 v81, v209, v210
	v_cvt_pk_bf16_f32 v82, v211, v220
	v_cvt_pk_bf16_f32 v83, v221, v222
	v_cvt_pk_bf16_f32 v84, v223, v224
	v_cvt_pk_bf16_f32 v85, v225, v226
	v_cvt_pk_bf16_f32 v86, v227, v228
	v_cvt_pk_bf16_f32 v87, v229, v230
	v_cvt_pk_bf16_f32 v88, v201, v202
	v_cvt_pk_bf16_f32 v89, v203, v204
	v_cvt_pk_bf16_f32 v90, v205, v206
	v_cvt_pk_bf16_f32 v91, v207, v231
	v_cvt_pk_bf16_f32 v92, v232, v233
	v_cvt_pk_bf16_f32 v93, v234, v235
	v_cvt_pk_bf16_f32 v94, v236, v237
	v_cvt_pk_bf16_f32 v95, v238, v95
	s_add_i32 m0, s84, 0x4400
	s_add_u32 s66, s78, s65
	s_addc_u32 s67, s79, 0
	global_load_lds_dwordx4 v185, s[66:67]
	s_add_i32 m0, s84, 0x6400
	s_add_i32 s64, s65, 0x60000
	global_load_lds_dwordx4 v184, s[66:67]
	s_cmp_eq_u32 s55, 29
	s_cselect_b32 s64, s89, s64
	s_add_i32 m0, s84, 0x14400
	s_add_u32 s70, s80, s64
	s_addc_u32 s71, s81, 0
	global_load_lds_dwordx4 v183, s[70:71]
	s_add_i32 m0, s84, 0x16400
	s_mov_b32 s65, s64
	global_load_lds_dwordx4 v182, s[70:71]

.LBB0_803:
	s_waitcnt vmcnt(0)
	s_barrier
	v_exp_f32_e32 v159, v96
	v_exp_f32_e32 v161, v97
	v_exp_f32_e32 v157, v98
	v_exp_f32_e32 v160, v99
	v_exp_f32_e32 v155, v100
	v_exp_f32_e32 v158, v101
	v_exp_f32_e32 v154, v102
	v_exp_f32_e32 v156, v103
	v_exp_f32_e32 v151, v104
	v_exp_f32_e32 v153, v105
	v_exp_f32_e32 v149, v106
	v_exp_f32_e32 v152, v107
	v_exp_f32_e32 v147, v108
	v_exp_f32_e32 v150, v109
	v_exp_f32_e32 v146, v110
	v_exp_f32_e32 v148, v111
	v_add_u32_e32 v180, 0x8000, v194
	v_add_u32_e32 v134, s20, v189
	v_add_u32_e32 v84, v134, v190
	ds_read_b128 v[80:83], v84 offset:50176
	ds_read_b128 v[84:87], v84 offset:58368
	v_add_u32_e32 v130, v134, v188
	v_exp_f32_e32 v78, v78
	v_exp_f32_e32 v79, v79
	s_waitcnt lgkmcnt(1)
	v_mfma_f32_32x32x16_bf16 v[96:111], v[80:83], v[122:125], 0
	s_waitcnt lgkmcnt(0)
	v_mfma_f32_32x32x16_bf16 v[80:95], v[84:87], v[122:125], 0
	ds_read_b128 v[122:125], v130 offset:50176
	ds_read_b128 v[130:133], v130 offset:58368
	s_waitcnt lgkmcnt(1)
	v_mfma_f32_32x32x16_bf16 v[96:111], v[122:125], v[126:129], v[96:111]
	s_waitcnt lgkmcnt(0)
	v_mfma_f32_32x32x16_bf16 v[80:95], v[130:133], v[126:129], v[80:95]
	v_add_u32_e32 v126, v134, v187
	ds_read_b128 v[122:125], v126 offset:50176
	ds_read_b128 v[126:129], v126 offset:58368
	s_waitcnt lgkmcnt(1)
	v_mfma_f32_32x32x16_bf16 v[96:111], v[122:125], v[118:121], v[96:111]
	v_add_u32_e32 v122, v134, v186
	s_waitcnt lgkmcnt(0)
	v_mfma_f32_32x32x16_bf16 v[80:95], v[126:129], v[118:121], v[80:95]
	ds_read_b128 v[118:121], v122 offset:50176
	ds_read_b128 v[122:125], v122 offset:58368
	v_exp_f32_e32 v126, v76
	v_exp_f32_e32 v127, v77
	s_waitcnt lgkmcnt(1)
	v_mfma_f32_32x32x16_bf16 v[96:111], v[118:121], v[114:117], v[96:111]
	v_exp_f32_e32 v118, v68
	v_exp_f32_e32 v119, v69
	v_exp_f32_e32 v120, v70
	v_exp_f32_e32 v121, v71
	s_waitcnt lgkmcnt(0)
	v_mfma_f32_32x32x16_bf16 v[80:95], v[122:125], v[114:117], v[80:95]
	v_exp_f32_e32 v114, v64
	v_add_f32_e32 v64, 0, v159
	v_add_f32_e32 v64, v161, v64
	v_add_f32_e32 v64, v157, v64
	v_add_f32_e32 v64, v160, v64
	v_add_f32_e32 v64, v155, v64
	v_add_f32_e32 v64, v158, v64
	v_add_f32_e32 v64, v154, v64
	v_add_f32_e32 v64, v156, v64
	v_add_f32_e32 v64, v151, v64
	v_add_f32_e32 v64, v153, v64
	v_add_f32_e32 v64, v149, v64
	v_add_f32_e32 v64, v152, v64
	v_add_f32_e32 v64, v147, v64
	v_exp_f32_e32 v115, v65
	v_add_f32_e32 v64, v150, v64
	v_exp_f32_e32 v116, v66
	v_add_f32_e32 v64, v146, v64
	v_exp_f32_e32 v117, v67
	v_add_f32_e32 v64, v148, v64
	v_add_f32_e32 v64, v114, v64
	v_add_f32_e32 v64, v115, v64
	v_add_f32_e32 v64, v116, v64
	v_add_f32_e32 v64, v117, v64
	v_exp_f32_e32 v122, v72
	v_add_f32_e32 v64, v118, v64
	v_exp_f32_e32 v123, v73
	v_add_f32_e32 v64, v119, v64
	v_exp_f32_e32 v124, v74
	v_add_f32_e32 v64, v120, v64
	v_exp_f32_e32 v125, v75
	v_add_f32_e32 v64, v121, v64
	v_add_f32_e32 v64, v122, v64
	v_add_f32_e32 v64, v123, v64
	v_add_f32_e32 v64, v124, v64
	v_add_f32_e32 v64, v125, v64
	v_add_f32_e32 v64, v126, v64
	v_add_f32_e32 v64, v127, v64
	v_add_f32_e32 v64, v78, v64
	v_add_f32_e32 v64, v79, v64
	v_cvt_pk_bf16_f32 v66, v159, v161
	v_cvt_pk_bf16_f32 v67, v157, v160
	v_cvt_pk_bf16_f32 v68, v155, v158
	v_cvt_pk_bf16_f32 v69, v154, v156
	v_cvt_pk_bf16_f32 v70, v151, v153
	v_cvt_pk_bf16_f32 v71, v149, v152
	v_cvt_pk_bf16_f32 v72, v147, v150
	v_cvt_pk_bf16_f32 v73, v146, v148
	v_cvt_pk_bf16_f32 v74, v114, v115
	v_cvt_pk_bf16_f32 v75, v116, v117
	v_cvt_pk_bf16_f32 v76, v118, v119
	v_cvt_pk_bf16_f32 v77, v120, v121
	v_cvt_pk_bf16_f32 v114, v122, v123
	v_cvt_pk_bf16_f32 v115, v124, v125
	v_cvt_pk_bf16_f32 v116, v126, v127
	v_cvt_pk_bf16_f32 v117, v78, v79
	s_nop 0
	s_add_i32 s0, 0, 0x4400
	v_add_u32_e32 v78, s0, v192
	ds_read_b64_tr_b16 v[118:119], v78 offset:0
	ds_read_b64_tr_b16 v[120:121], v78 offset:0x800
	ds_read_b64_tr_b16 v[122:123], v78 offset:0x1000
	ds_read_b64_tr_b16 v[124:125], v78 offset:0x1800
	ds_read_b64_tr_b16 v[126:127], v78 offset:0x2000
	ds_read_b64_tr_b16 v[128:129], v78 offset:0x2800
	ds_read_b64_tr_b16 v[130:131], v78 offset:0x3000
	ds_read_b64_tr_b16 v[132:133], v78 offset:0x3800
	s_waitcnt lgkmcnt(0)
	s_nop 0
	v_mfma_f32_32x32x16_bf16 v[0:15], v[66:69], v[118:121], v[0:15]
	ds_read_b64_tr_b16 v[118:119], v78 offset:0x200
	ds_read_b64_tr_b16 v[120:121], v78 offset:0xa00
	v_mfma_f32_32x32x16_bf16 v[0:15], v[70:73], v[122:125], v[0:15]
	ds_read_b64_tr_b16 v[122:123], v78 offset:0x1200
	ds_read_b64_tr_b16 v[124:125], v78 offset:0x1a00
	v_mfma_f32_32x32x16_bf16 v[0:15], v[74:77], v[126:129], v[0:15]
	ds_read_b64_tr_b16 v[126:127], v78 offset:0x2200
	ds_read_b64_tr_b16 v[128:129], v78 offset:0x2a00
	v_mfma_f32_32x32x16_bf16 v[0:15], v[114:117], v[130:133], v[0:15]
	ds_read_b64_tr_b16 v[130:131], v78 offset:0x3200
	ds_read_b64_tr_b16 v[132:133], v78 offset:0x3a00
	s_waitcnt lgkmcnt(0)
	v_mfma_f32_32x32x16_bf16 v[48:63], v[66:69], v[118:121], v[48:63]
	ds_read_b64_tr_b16 v[118:119], v78 offset:0x400
	ds_read_b64_tr_b16 v[120:121], v78 offset:0xc00
	v_mfma_f32_32x32x16_bf16 v[48:63], v[70:73], v[122:125], v[48:63]
	ds_read_b64_tr_b16 v[122:123], v78 offset:0x1400
	ds_read_b64_tr_b16 v[124:125], v78 offset:0x1c00
	v_mfma_f32_32x32x16_bf16 v[48:63], v[74:77], v[126:129], v[48:63]
	ds_read_b64_tr_b16 v[126:127], v78 offset:0x2400
	ds_read_b64_tr_b16 v[128:129], v78 offset:0x2c00
	v_mfma_f32_32x32x16_bf16 v[48:63], v[114:117], v[130:133], v[48:63]
	ds_read_b64_tr_b16 v[130:131], v78 offset:0x3400
	ds_read_b64_tr_b16 v[132:133], v78 offset:0x3c00
	s_waitcnt lgkmcnt(0)
	v_mfma_f32_32x32x16_bf16 v[32:47], v[66:69], v[118:121], v[32:47]
	ds_read_b64_tr_b16 v[118:119], v78 offset:0x600
	ds_read_b64_tr_b16 v[120:121], v78 offset:0xe00
	v_mfma_f32_32x32x16_bf16 v[32:47], v[70:73], v[122:125], v[32:47]
	ds_read_b64_tr_b16 v[122:123], v78 offset:0x1600
	ds_read_b64_tr_b16 v[124:125], v78 offset:0x1e00
	v_mfma_f32_32x32x16_bf16 v[32:47], v[74:77], v[126:129], v[32:47]
	ds_read_b64_tr_b16 v[126:127], v78 offset:0x2600
	ds_read_b64_tr_b16 v[128:129], v78 offset:0x2e00
	v_mfma_f32_32x32x16_bf16 v[32:47], v[114:117], v[130:133], v[32:47]
	ds_read_b64_tr_b16 v[130:131], v78 offset:0x3600
	ds_read_b64_tr_b16 v[132:133], v78 offset:0x3e00
	s_waitcnt lgkmcnt(0)
	v_mfma_f32_32x32x16_bf16 v[16:31], v[66:69], v[118:121], v[16:31]
	v_max_f32_e32 v66, v97, v97
	v_max_f32_e32 v67, v96, v96
	v_max_f32_e32 v66, v67, v66
	v_max3_f32 v66, v66, v98, v99
	v_max3_f32 v66, v66, v100, v101
	v_max3_f32 v66, v66, v102, v103
	v_max3_f32 v66, v66, v104, v105
	v_mfma_f32_32x32x16_bf16 v[16:31], v[70:73], v[122:125], v[16:31]
	v_max3_f32 v66, v66, v106, v107
	v_max3_f32 v66, v66, v108, v109
	v_max3_f32 v66, v66, v110, v111
	v_max3_f32 v66, v66, v80, v81
	v_max3_f32 v66, v66, v82, v83
	v_max3_f32 v66, v66, v84, v85
	v_max3_f32 v66, v66, v86, v87
	v_mfma_f32_32x32x16_bf16 v[16:31], v[74:77], v[126:129], v[16:31]
	v_max3_f32 v66, v66, v88, v89
	v_max3_f32 v66, v66, v90, v91
	v_max3_f32 v66, v66, v92, v93
	v_max3_f32 v66, v66, v94, v95
	v_mov_b32_e32 v67, v66
	s_nop 1
	v_permlane32_swap_b32_e32 v66, v67
	v_mfma_f32_32x32x16_bf16 v[16:31], v[114:117], v[130:133], v[16:31]
	v_max_f32_e32 v67, v67, v67
	v_max_f32_e32 v66, v66, v66
	v_max_f32_e32 v67, v66, v67
	v_cmp_eq_f32_e32 vcc, 0, v164
	v_cmp_ge_f32_e64 s[40:41], s75, v67
	s_and_b64 s[0:1], vcc, s[40:41]
	v_cndmask_b32_e64 v66, 0, 1, s[0:1]
	v_cmp_ne_u32_e32 vcc, 0, v66
	s_cmp_eq_u64 vcc, exec
	v_mov_b32_e32 v66, 1.0
	s_cbranch_scc0 .LBB0_815
	v_cmp_gt_f32_e32 vcc, 1.0, v66
	s_cbranch_vccz .LBB0_808
